# same as ring-16 hybrid but adjacency loads use the default cache policy instead of nt
# baseline (speedup 1.0000x reference)
.Lk1_scan:
	s_load_dwordx2 s[4:5], s[0:1], 0x0
	s_load_dwordx4 s[8:11], s[0:1], 0x20
	s_load_dwordx2 s[12:13], s[0:1], 0x30
	v_and_b32_e32 v6, 63, v0
	v_readfirstlane_b32 s3, v0
	v_lshlrev_b32_e32 v1, 4, v6
	v_lshlrev_b32_e32 v2, 2, v6
	v_or_b32_e32 v3, 1, v2
	v_or_b32_e32 v4, 2, v2
	v_or_b32_e32 v5, 3, v2
	s_lshr_b32 s3, s3, 6
	s_sub_u32 s16, s2, 0x60
	s_lshl_b32 s16, s16, 2
	s_add_u32 s16, s16, s3
	s_mul_i32 s17, s16, 0x48000
	s_lshr_b32 s18, s17, 2
	s_lshl_b32 s24, s3, 13
	s_mov_b32 s25, s24
	s_mov_b32 s28, s24
	s_mov_b32 s36, 0
	s_mov_b64 s[62:63], 0
	v_mov_b32_e32 v21, 1
	s_mov_b32 s27, 0
	s_mov_b32 s29, 0x55555556
	s_mov_b32 s31, 0xc0000
	s_waitcnt lgkmcnt(0)
	s_and_b32 s50, s16, 15
	s_mul_i32 s52, s50, 512
	s_add_u32 s52, s52, 28672
	s_lshl_b32 s53, s50, 6
	s_add_u32 s53, s53, 0xe000
	s_add_u32 s54, s10, s53
	s_addc_u32 s55, s11, 0
	s_mul_i32 s59, s16, 14
	s_mul_i32 s57, s59, 0x4000
	s_lshr_b32 s18, s57, 2
	s_add_u32 s6, s4, s57
	s_addc_u32 s7, s5, 0
	v_mov_b32_e32 v27, 0
	global_load_dwordx4 v[28:31], v1, s[6:7]
	s_add_u32 s6, s6, 0x400
	s_addc_u32 s7, s7, 0
	global_load_dwordx4 v[32:35], v1, s[6:7]
	s_add_u32 s6, s6, 0x400
	s_addc_u32 s7, s7, 0
	global_load_dwordx4 v[36:39], v1, s[6:7]
	s_add_u32 s6, s6, 0x400
	s_addc_u32 s7, s7, 0
	global_load_dwordx4 v[40:43], v1, s[6:7]
	s_add_u32 s6, s6, 0x400
	s_addc_u32 s7, s7, 0
	global_load_dwordx4 v[44:47], v1, s[6:7]
	s_add_u32 s6, s6, 0x400
	s_addc_u32 s7, s7, 0
	global_load_dwordx4 v[48:51], v1, s[6:7]
	s_add_u32 s6, s6, 0x400
	s_addc_u32 s7, s7, 0
	global_load_dwordx4 v[52:55], v1, s[6:7]
	s_add_u32 s6, s6, 0x400
	s_addc_u32 s7, s7, 0
	global_load_dwordx4 v[56:59], v1, s[6:7]
	s_add_u32 s6, s6, 0x400
	s_addc_u32 s7, s7, 0
	global_load_dwordx4 v[60:63], v1, s[6:7]
	s_add_u32 s6, s6, 0x400
	s_addc_u32 s7, s7, 0
	global_load_dwordx4 v[64:67], v1, s[6:7]
	s_add_u32 s6, s6, 0x400
	s_addc_u32 s7, s7, 0
	global_load_dwordx4 v[68:71], v1, s[6:7]
	s_add_u32 s6, s6, 0x400
	s_addc_u32 s7, s7, 0
	global_load_dwordx4 v[72:75], v1, s[6:7]
	s_add_u32 s6, s6, 0x400
	s_addc_u32 s7, s7, 0
	global_load_dwordx4 v[76:79], v1, s[6:7]
	s_add_u32 s6, s6, 0x400
	s_addc_u32 s7, s7, 0
	global_load_dwordx4 v[80:83], v1, s[6:7]
	s_add_u32 s6, s6, 0x400
	s_addc_u32 s7, s7, 0
	global_load_dwordx4 v[84:87], v1, s[6:7]
	s_add_u32 s6, s6, 0x400
	s_addc_u32 s7, s7, 0
	global_load_dwordx4 v[88:91], v1, s[6:7]
	s_add_u32 s6, s6, 0x400
	s_addc_u32 s7, s7, 0
	s_mov_b32 s26, 18
	s_add_u32 s57, s59, 1
	s_mul_i32 s57, s57, 0x4000
	s_lshr_b32 s58, s57, 2
	s_add_u32 s6, s4, s57
	s_addc_u32 s7, s5, 0
	s_mov_b32 s26, 0

.Lk1_contm_7:
	global_load_dwordx4 v[28:31], v1, s[6:7]
	s_add_u32 s6, s6, 0x400
	s_addc_u32 s7, s7, 0
	global_load_dwordx4 v[32:35], v1, s[6:7]
	s_add_u32 s6, s6, 0x400
	s_addc_u32 s7, s7, 0
	global_load_dwordx4 v[36:39], v1, s[6:7]
	s_add_u32 s6, s6, 0x400
	s_addc_u32 s7, s7, 0
	global_load_dwordx4 v[40:43], v1, s[6:7]
	s_add_u32 s6, s6, 0x400
	s_addc_u32 s7, s7, 0
	global_load_dwordx4 v[44:47], v1, s[6:7]
	s_add_u32 s6, s6, 0x400
	s_addc_u32 s7, s7, 0
	global_load_dwordx4 v[48:51], v1, s[6:7]
	s_add_u32 s6, s6, 0x400
	s_addc_u32 s7, s7, 0
	global_load_dwordx4 v[52:55], v1, s[6:7]
	s_add_u32 s6, s6, 0x400
	s_addc_u32 s7, s7, 0
	global_load_dwordx4 v[56:59], v1, s[6:7]
	s_add_u32 s6, s6, 0x400
	s_addc_u32 s7, s7, 0
	s_waitcnt vmcnt(15)
	v_or3_b32 v12, v60, v61, v62
	v_or_b32_e32 v12, v12, v63
	v_cmp_ne_u32_e32 vcc, 0, v12
	s_cbranch_vccnz .Lk1_hitm_8

.Lk1_contm_15:
	global_load_dwordx4 v[60:63], v1, s[6:7]
	s_add_u32 s6, s6, 0x400
	s_addc_u32 s7, s7, 0
	global_load_dwordx4 v[64:67], v1, s[6:7]
	s_add_u32 s6, s6, 0x400
	s_addc_u32 s7, s7, 0
	global_load_dwordx4 v[68:71], v1, s[6:7]
	s_add_u32 s6, s6, 0x400
	s_addc_u32 s7, s7, 0
	global_load_dwordx4 v[72:75], v1, s[6:7]
	s_add_u32 s6, s6, 0x400
	s_addc_u32 s7, s7, 0
	global_load_dwordx4 v[76:79], v1, s[6:7]
	s_add_u32 s6, s6, 0x400
	s_addc_u32 s7, s7, 0
	global_load_dwordx4 v[80:83], v1, s[6:7]
	s_add_u32 s6, s6, 0x400
	s_addc_u32 s7, s7, 0
	global_load_dwordx4 v[84:87], v1, s[6:7]
	s_add_u32 s6, s6, 0x400
	s_addc_u32 s7, s7, 0
	global_load_dwordx4 v[88:91], v1, s[6:7]
	s_add_u32 s6, s6, 0x400
	s_addc_u32 s7, s7, 0
	s_mov_b32 s18, s58
	s_add_u32 s60, s26, 2
	s_cmp_lt_u32 s60, 14
	s_cbranch_scc0 .Lk1_dynid
	s_add_u32 s57, s59, s60
	s_branch .Lk1_haveid
